# l3sleep2
# speedup vs baseline: 1.0164x; 1.0043x over previous
.LBB1_3:
	s_and_b32 s8, s55, 6
	ds_read_b128 v[114:117], v77
	ds_read_b128 v[118:121], v77 offset:512
	ds_read_b128 v[122:125], v77 offset:1024
	ds_read_b128 v[126:129], v77 offset:1536
	ds_read_b64 v[90:91], v78
	ds_read_b64 v[92:93], v78 offset:8
	ds_read_b64 v[94:95], v78 offset:16
	ds_read_b64 v[96:97], v81
	ds_read_b64 v[98:99], v81 offset:8
	ds_read_b64 v[100:101], v81 offset:16
	v_lshl_add_u32 v89, s8, 9, v87
	ds_read_u16 v154, v89
	ds_read_b128 v[130:133], v77 offset:8192
	ds_read_b128 v[134:137], v77 offset:8704
	ds_read_b128 v[138:141], v77 offset:9216
	ds_read_b128 v[142:145], v77 offset:9728
	ds_read_b64 v[102:103], v80
	ds_read_b64 v[104:105], v80 offset:8
	ds_read_b64 v[106:107], v80 offset:16
	s_mov_b32 m0, s50
	ds_read_b64 v[108:109], v79
	ds_read_b64 v[110:111], v79 offset:8
	ds_read_b64 v[112:113], v79 offset:16
	ds_read_u16 v89, v89 offset:512
	global_load_lds_dwordx4 v161, s[72:73]
	s_mov_b32 m0, s51
	s_add_i32 s56, s37, s55
	global_load_lds_dwordx4 v162, s[72:73]
	s_mov_b32 m0, s52
	s_add_i32 s8, s56, 4
	global_load_lds_dwordx4 v167, s[76:77]
	s_mov_b32 m0, s53
	s_min_u32 s57, s8, 63
	global_load_lds_dwordx4 v168, s[76:77]
	s_mov_b32 m0, s54
	s_lshl_b32 s8, s57, 10
	global_load_lds_dwordx4 v169, s[76:77]
	s_add_u32 s82, s80, s8
	s_addc_u32 s83, s81, 0
	s_lshl_b32 s8, s57, 9
	s_and_b32 s8, s8, 0xe00
	s_add_i32 m0, s49, s8
	s_add_i32 s57, s55, 4
	global_load_lds_dword v160, s[82:83]
	s_sleep 2
	s_waitcnt vmcnt(6)
	s_waitcnt lgkmcnt(0)
	s_barrier
	s_setprio 1
	s_waitcnt lgkmcnt(0)
	v_mfma_scale_f32_32x32x64_f8f6f4 v[50:65], v[90:95], v[114:117], v[50:65], v154, v88 op_sel_hi:[0,0,0] cbsz:2 blgp:4
	v_mfma_scale_f32_32x32x64_f8f6f4 v[34:49], v[90:95], v[118:121], v[34:49], v154, v88 op_sel_hi:[0,0,0] cbsz:2 blgp:4
	v_mfma_scale_f32_32x32x64_f8f6f4 v[18:33], v[90:95], v[122:125], v[18:33], v154, v88 op_sel_hi:[0,0,0] cbsz:2 blgp:4
	v_mfma_scale_f32_32x32x64_f8f6f4 v[2:17], v[90:95], v[126:129], v[2:17], v154, v88 op_sel_hi:[0,0,0] cbsz:2 blgp:4
	v_mfma_scale_f32_32x32x64_f8f6f4 v[50:65], v[96:101], v[114:117], v[50:65], v154, v88 op_sel:[1,0,0] op_sel_hi:[0,0,0] cbsz:2 blgp:4
	v_mfma_scale_f32_32x32x64_f8f6f4 v[34:49], v[96:101], v[118:121], v[34:49], v154, v88 op_sel:[1,0,0] op_sel_hi:[0,0,0] cbsz:2 blgp:4
	v_mfma_scale_f32_32x32x64_f8f6f4 v[18:33], v[96:101], v[122:125], v[18:33], v154, v88 op_sel:[1,0,0] op_sel_hi:[0,0,0] cbsz:2 blgp:4
	v_mfma_scale_f32_32x32x64_f8f6f4 v[2:17], v[96:101], v[126:129], v[2:17], v154, v88 op_sel:[1,0,0] op_sel_hi:[0,0,0] cbsz:2 blgp:4
	v_mfma_scale_f32_32x32x64_f8f6f4 v[50:65], v[102:107], v[130:133], v[50:65], v89, v88 op_sel_hi:[0,0,0] cbsz:2 blgp:4
	v_mfma_scale_f32_32x32x64_f8f6f4 v[34:49], v[102:107], v[134:137], v[34:49], v89, v88 op_sel_hi:[0,0,0] cbsz:2 blgp:4
	v_mfma_scale_f32_32x32x64_f8f6f4 v[18:33], v[102:107], v[138:141], v[18:33], v89, v88 op_sel_hi:[0,0,0] cbsz:2 blgp:4
	v_mfma_scale_f32_32x32x64_f8f6f4 v[2:17], v[102:107], v[142:145], v[2:17], v89, v88 op_sel_hi:[0,0,0] cbsz:2 blgp:4
	v_mfma_scale_f32_32x32x64_f8f6f4 v[50:65], v[108:113], v[130:133], v[50:65], v89, v88 op_sel:[1,0,0] op_sel_hi:[0,0,0] cbsz:2 blgp:4
	v_mfma_scale_f32_32x32x64_f8f6f4 v[34:49], v[108:113], v[134:137], v[34:49], v89, v88 op_sel:[1,0,0] op_sel_hi:[0,0,0] cbsz:2 blgp:4
	v_mfma_scale_f32_32x32x64_f8f6f4 v[18:33], v[108:113], v[138:141], v[18:33], v89, v88 op_sel:[1,0,0] op_sel_hi:[0,0,0] cbsz:2 blgp:4
	v_mfma_scale_f32_32x32x64_f8f6f4 v[2:17], v[108:113], v[142:145], v[2:17], v89, v88 op_sel:[1,0,0] op_sel_hi:[0,0,0] cbsz:2 blgp:4
	s_setprio 0
	s_barrier
	s_add_i32 s8, s55, 2
	s_and_b32 s8, s8, 6
	ds_read_b128 v[114:117], v77 offset:40960
	ds_read_b128 v[118:121], v77 offset:41472
	ds_read_b128 v[122:125], v77 offset:41984
	ds_read_b128 v[126:129], v77 offset:42496
	ds_read_b64 v[90:91], v75
	ds_read_b64 v[92:93], v75 offset:8
	ds_read_b64 v[94:95], v75 offset:16
	ds_read_b64 v[96:97], v76
	ds_read_b64 v[98:99], v76 offset:8
	ds_read_b64 v[100:101], v76 offset:16
	v_lshl_add_u32 v89, s8, 9, v87
	ds_read_u16 v154, v89
	ds_read_b128 v[130:133], v77 offset:49152
	ds_read_b128 v[134:137], v77 offset:49664
	ds_read_b128 v[138:141], v77 offset:50176
	ds_read_b128 v[142:145], v77 offset:50688
	ds_read_b64 v[102:103], v74
	ds_read_b64 v[104:105], v74 offset:8
	ds_read_b64 v[106:107], v74 offset:16
	s_mov_b32 m0, s38
	ds_read_b64 v[108:109], v73
	ds_read_b64 v[110:111], v73 offset:8
	ds_read_b64 v[112:113], v73 offset:16
	ds_read_u16 v89, v89 offset:512
	global_load_lds_dwordx4 v163, s[72:73]
	s_mov_b32 m0, s39
	s_add_i32 s8, s56, 6
	global_load_lds_dwordx4 v164, s[72:73]
	s_mov_b32 m0, s40
	s_min_u32 s58, s8, 63
	global_load_lds_dwordx4 v170, s[76:77]
	s_mov_b32 m0, s41
	s_lshl_b32 s8, s58, 10
	global_load_lds_dwordx4 v171, s[76:77]
	s_mov_b32 m0, s42
	s_nop 0
	global_load_lds_dwordx4 v172, s[76:77]
	s_add_u32 s82, s80, s8
	s_addc_u32 s83, s81, 0
	s_lshl_b32 s8, s58, 9
	s_and_b32 s8, s8, 0xe00
	s_add_i32 m0, s49, s8
	s_nop 0
	global_load_lds_dword v160, s[82:83]
	s_sleep 2
	s_waitcnt vmcnt(6)
	s_waitcnt lgkmcnt(0)
	s_barrier
	s_setprio 1
	s_waitcnt lgkmcnt(0)
	v_mfma_scale_f32_32x32x64_f8f6f4 v[50:65], v[90:95], v[114:117], v[50:65], v154, v88 op_sel_hi:[0,0,0] cbsz:2 blgp:4
	v_mfma_scale_f32_32x32x64_f8f6f4 v[34:49], v[90:95], v[118:121], v[34:49], v154, v88 op_sel_hi:[0,0,0] cbsz:2 blgp:4
	v_mfma_scale_f32_32x32x64_f8f6f4 v[18:33], v[90:95], v[122:125], v[18:33], v154, v88 op_sel_hi:[0,0,0] cbsz:2 blgp:4
	v_mfma_scale_f32_32x32x64_f8f6f4 v[2:17], v[90:95], v[126:129], v[2:17], v154, v88 op_sel_hi:[0,0,0] cbsz:2 blgp:4
	v_mfma_scale_f32_32x32x64_f8f6f4 v[50:65], v[96:101], v[114:117], v[50:65], v154, v88 op_sel:[1,0,0] op_sel_hi:[0,0,0] cbsz:2 blgp:4
	v_mfma_scale_f32_32x32x64_f8f6f4 v[34:49], v[96:101], v[118:121], v[34:49], v154, v88 op_sel:[1,0,0] op_sel_hi:[0,0,0] cbsz:2 blgp:4
	v_mfma_scale_f32_32x32x64_f8f6f4 v[18:33], v[96:101], v[122:125], v[18:33], v154, v88 op_sel:[1,0,0] op_sel_hi:[0,0,0] cbsz:2 blgp:4
	v_mfma_scale_f32_32x32x64_f8f6f4 v[2:17], v[96:101], v[126:129], v[2:17], v154, v88 op_sel:[1,0,0] op_sel_hi:[0,0,0] cbsz:2 blgp:4
	v_mfma_scale_f32_32x32x64_f8f6f4 v[50:65], v[102:107], v[130:133], v[50:65], v89, v88 op_sel_hi:[0,0,0] cbsz:2 blgp:4
	v_mfma_scale_f32_32x32x64_f8f6f4 v[34:49], v[102:107], v[134:137], v[34:49], v89, v88 op_sel_hi:[0,0,0] cbsz:2 blgp:4
	v_mfma_scale_f32_32x32x64_f8f6f4 v[18:33], v[102:107], v[138:141], v[18:33], v89, v88 op_sel_hi:[0,0,0] cbsz:2 blgp:4
	v_mfma_scale_f32_32x32x64_f8f6f4 v[2:17], v[102:107], v[142:145], v[2:17], v89, v88 op_sel_hi:[0,0,0] cbsz:2 blgp:4
	v_mfma_scale_f32_32x32x64_f8f6f4 v[50:65], v[108:113], v[130:133], v[50:65], v89, v88 op_sel:[1,0,0] op_sel_hi:[0,0,0] cbsz:2 blgp:4
	v_mfma_scale_f32_32x32x64_f8f6f4 v[34:49], v[108:113], v[134:137], v[34:49], v89, v88 op_sel:[1,0,0] op_sel_hi:[0,0,0] cbsz:2 blgp:4
	v_mfma_scale_f32_32x32x64_f8f6f4 v[18:33], v[108:113], v[138:141], v[18:33], v89, v88 op_sel:[1,0,0] op_sel_hi:[0,0,0] cbsz:2 blgp:4
	v_mfma_scale_f32_32x32x64_f8f6f4 v[2:17], v[108:113], v[142:145], v[2:17], v89, v88 op_sel:[1,0,0] op_sel_hi:[0,0,0] cbsz:2 blgp:4
	s_setprio 0
	s_barrier
	s_and_b32 s8, s57, 6
	ds_read_b128 v[114:117], v86
	ds_read_b128 v[118:121], v86 offset:512
	ds_read_b128 v[122:125], v86 offset:1024
	ds_read_b128 v[126:129], v86 offset:1536
	ds_read_b64 v[90:91], v82
	ds_read_b64 v[92:93], v82 offset:8
	ds_read_b64 v[94:95], v82 offset:16
	ds_read_b64 v[96:97], v83
	ds_read_b64 v[98:99], v83 offset:8
	ds_read_b64 v[100:101], v83 offset:16
	v_lshl_add_u32 v89, s8, 9, v87
	ds_read_u16 v154, v89
	ds_read_b128 v[130:133], v86 offset:8192
	ds_read_b128 v[134:137], v86 offset:8704
	ds_read_b128 v[138:141], v86 offset:9216
	ds_read_b128 v[142:145], v86 offset:9728
	ds_read_b64 v[102:103], v84
	ds_read_b64 v[104:105], v84 offset:8
	ds_read_b64 v[106:107], v84 offset:16
	s_mov_b32 m0, s43
	ds_read_b64 v[108:109], v85
	ds_read_b64 v[110:111], v85 offset:8
	ds_read_b64 v[112:113], v85 offset:16
	ds_read_u16 v89, v89 offset:512
	global_load_lds_dwordx4 v165, s[72:73]
	s_mov_b32 m0, s44
	s_nop 0
	global_load_lds_dwordx4 v166, s[72:73]
	s_mov_b32 m0, s45
	s_add_i32 s56, s56, 8
	global_load_lds_dwordx4 v173, s[76:77]
	s_mov_b32 m0, s46
	s_min_u32 s56, s56, 63
	global_load_lds_dwordx4 v174, s[76:77]
	s_mov_b32 m0, s47
	s_lshl_b32 s8, s56, 10
	global_load_lds_dwordx4 v175, s[76:77]
	s_add_u32 s82, s80, s8
	s_addc_u32 s83, s81, 0
	s_lshl_b32 s8, s56, 9
	s_and_b32 s8, s8, 0xe00
	s_add_i32 m0, s49, s8
	s_nop 0
	global_load_lds_dword v160, s[82:83]
	s_sleep 2
	s_waitcnt vmcnt(6)
	s_waitcnt lgkmcnt(0)
	s_barrier
	s_setprio 1
	s_waitcnt lgkmcnt(0)
	v_mfma_scale_f32_32x32x64_f8f6f4 v[50:65], v[90:95], v[114:117], v[50:65], v154, v88 op_sel_hi:[0,0,0] cbsz:2 blgp:4
	v_mfma_scale_f32_32x32x64_f8f6f4 v[34:49], v[90:95], v[118:121], v[34:49], v154, v88 op_sel_hi:[0,0,0] cbsz:2 blgp:4
	v_mfma_scale_f32_32x32x64_f8f6f4 v[18:33], v[90:95], v[122:125], v[18:33], v154, v88 op_sel_hi:[0,0,0] cbsz:2 blgp:4
	v_mfma_scale_f32_32x32x64_f8f6f4 v[2:17], v[90:95], v[126:129], v[2:17], v154, v88 op_sel_hi:[0,0,0] cbsz:2 blgp:4
	v_mfma_scale_f32_32x32x64_f8f6f4 v[50:65], v[96:101], v[114:117], v[50:65], v154, v88 op_sel:[1,0,0] op_sel_hi:[0,0,0] cbsz:2 blgp:4
	v_mfma_scale_f32_32x32x64_f8f6f4 v[34:49], v[96:101], v[118:121], v[34:49], v154, v88 op_sel:[1,0,0] op_sel_hi:[0,0,0] cbsz:2 blgp:4
	v_mfma_scale_f32_32x32x64_f8f6f4 v[18:33], v[96:101], v[122:125], v[18:33], v154, v88 op_sel:[1,0,0] op_sel_hi:[0,0,0] cbsz:2 blgp:4
	v_mfma_scale_f32_32x32x64_f8f6f4 v[2:17], v[96:101], v[126:129], v[2:17], v154, v88 op_sel:[1,0,0] op_sel_hi:[0,0,0] cbsz:2 blgp:4
	v_mfma_scale_f32_32x32x64_f8f6f4 v[50:65], v[102:107], v[130:133], v[50:65], v89, v88 op_sel_hi:[0,0,0] cbsz:2 blgp:4
	v_mfma_scale_f32_32x32x64_f8f6f4 v[34:49], v[102:107], v[134:137], v[34:49], v89, v88 op_sel_hi:[0,0,0] cbsz:2 blgp:4
	v_mfma_scale_f32_32x32x64_f8f6f4 v[18:33], v[102:107], v[138:141], v[18:33], v89, v88 op_sel_hi:[0,0,0] cbsz:2 blgp:4
	v_mfma_scale_f32_32x32x64_f8f6f4 v[2:17], v[102:107], v[142:145], v[2:17], v89, v88 op_sel_hi:[0,0,0] cbsz:2 blgp:4
	v_mfma_scale_f32_32x32x64_f8f6f4 v[50:65], v[108:113], v[130:133], v[50:65], v89, v88 op_sel:[1,0,0] op_sel_hi:[0,0,0] cbsz:2 blgp:4
	v_mfma_scale_f32_32x32x64_f8f6f4 v[34:49], v[108:113], v[134:137], v[34:49], v89, v88 op_sel:[1,0,0] op_sel_hi:[0,0,0] cbsz:2 blgp:4
	v_mfma_scale_f32_32x32x64_f8f6f4 v[18:33], v[108:113], v[138:141], v[18:33], v89, v88 op_sel:[1,0,0] op_sel_hi:[0,0,0] cbsz:2 blgp:4
	v_mfma_scale_f32_32x32x64_f8f6f4 v[2:17], v[108:113], v[142:145], v[2:17], v89, v88 op_sel:[1,0,0] op_sel_hi:[0,0,0] cbsz:2 blgp:4
	s_setprio 0
	s_barrier
	s_add_i32 s48, s48, 3
	s_add_i32 s55, s55, 6
	s_add_u32 s72, s72, 0xc000
	s_addc_u32 s73, s73, 0
	s_add_u32 s76, s76, 0x24000
	s_addc_u32 s77, s77, 0
	s_cmp_lt_u32 s48, 27
	s_cbranch_scc1 .LBB1_3
	ds_read_b128 v[66:69], v77
	ds_read_b128 v[106:109], v77 offset:512
	ds_read_b128 v[110:113], v77 offset:1024
	ds_read_b128 v[114:117], v77 offset:1536
	ds_read_b64 v[82:83], v78
	ds_read_b64 v[84:85], v78 offset:8
	ds_read_b64 v[86:87], v78 offset:16
	ds_read_b64 v[88:89], v81
	ds_read_b64 v[90:91], v81 offset:8
	ds_read_b64 v[92:93], v81 offset:16
	v_add_u32_e32 v0, 0x1e800, v72
	ds_read_u16 v0, v0
	ds_read_b128 v[118:121], v77 offset:8192
	ds_read_b128 v[122:125], v77 offset:8704
	ds_read_b128 v[126:129], v77 offset:9216
	ds_read_b128 v[130:133], v77 offset:9728
	ds_read_b64 v[94:95], v80
	ds_read_b64 v[96:97], v80 offset:8
	ds_read_b64 v[98:99], v80 offset:16
	ds_read_b64 v[100:101], v79
	ds_read_b64 v[102:103], v79 offset:8
	ds_read_b64 v[104:105], v79 offset:16
	v_add_u32_e32 v1, 0x1ea00, v72
	ds_read_u16 v1, v1
	s_waitcnt vmcnt(0)
	s_waitcnt lgkmcnt(0)
	s_barrier
	s_setprio 1
	v_mov_b32_e32 v134, 0x7f7f7f7f
	s_waitcnt lgkmcnt(0)
	s_nop 0
	v_mfma_scale_f32_32x32x64_f8f6f4 v[50:65], v[82:87], v[66:69], v[50:65], v0, v134 op_sel_hi:[0,0,0] cbsz:2 blgp:4
	v_mfma_scale_f32_32x32x64_f8f6f4 v[34:49], v[82:87], v[106:109], v[34:49], v0, v134 op_sel_hi:[0,0,0] cbsz:2 blgp:4
	v_mfma_scale_f32_32x32x64_f8f6f4 v[18:33], v[82:87], v[110:113], v[18:33], v0, v134 op_sel_hi:[0,0,0] cbsz:2 blgp:4
	v_mfma_scale_f32_32x32x64_f8f6f4 v[2:17], v[82:87], v[114:117], v[2:17], v0, v134 op_sel_hi:[0,0,0] cbsz:2 blgp:4
	v_mfma_scale_f32_32x32x64_f8f6f4 v[50:65], v[88:93], v[66:69], v[50:65], v0, v134 op_sel:[1,0,0] op_sel_hi:[0,0,0] cbsz:2 blgp:4
	v_mfma_scale_f32_32x32x64_f8f6f4 v[34:49], v[88:93], v[106:109], v[34:49], v0, v134 op_sel:[1,0,0] op_sel_hi:[0,0,0] cbsz:2 blgp:4
	v_mfma_scale_f32_32x32x64_f8f6f4 v[18:33], v[88:93], v[110:113], v[18:33], v0, v134 op_sel:[1,0,0] op_sel_hi:[0,0,0] cbsz:2 blgp:4
	v_mfma_scale_f32_32x32x64_f8f6f4 v[2:17], v[88:93], v[114:117], v[2:17], v0, v134 op_sel:[1,0,0] op_sel_hi:[0,0,0] cbsz:2 blgp:4
	v_lshrrev_b32_e32 v0, 8, v1
	v_mfma_scale_f32_32x32x64_f8f6f4 v[50:65], v[94:99], v[118:121], v[50:65], v1, v134 op_sel_hi:[0,0,0] cbsz:2 blgp:4
	v_mfma_scale_f32_32x32x64_f8f6f4 v[34:49], v[94:99], v[122:125], v[34:49], v1, v134 op_sel_hi:[0,0,0] cbsz:2 blgp:4
	v_mfma_scale_f32_32x32x64_f8f6f4 v[18:33], v[94:99], v[126:129], v[18:33], v1, v134 op_sel_hi:[0,0,0] cbsz:2 blgp:4
	v_mfma_scale_f32_32x32x64_f8f6f4 v[2:17], v[94:99], v[130:133], v[2:17], v1, v134 op_sel_hi:[0,0,0] cbsz:2 blgp:4
	v_mfma_scale_f32_32x32x64_f8f6f4 v[50:65], v[100:105], v[118:121], v[50:65], v0, v134 op_sel_hi:[0,0,0] cbsz:2 blgp:4
	v_mfma_scale_f32_32x32x64_f8f6f4 v[34:49], v[100:105], v[122:125], v[34:49], v0, v134 op_sel_hi:[0,0,0] cbsz:2 blgp:4
	v_mfma_scale_f32_32x32x64_f8f6f4 v[18:33], v[100:105], v[126:129], v[18:33], v0, v134 op_sel_hi:[0,0,0] cbsz:2 blgp:4
	v_mfma_scale_f32_32x32x64_f8f6f4 v[2:17], v[100:105], v[130:133], v[2:17], v0, v134 op_sel_hi:[0,0,0] cbsz:2 blgp:4
	s_setprio 0
	s_barrier
	ds_read_b128 v[66:69], v77 offset:40960
	ds_read_b128 v[102:105], v77 offset:41472
	ds_read_b128 v[106:109], v77 offset:41984
	ds_read_b128 v[110:113], v77 offset:42496
	ds_read_b64 v[78:79], v75
	ds_read_b64 v[80:81], v75 offset:8
	ds_read_b64 v[82:83], v75 offset:16
	ds_read_b64 v[84:85], v76
	ds_read_b64 v[86:87], v76 offset:8
	ds_read_b64 v[88:89], v76 offset:16
	v_add_u32_e32 v0, 0x1ec00, v72
	ds_read_u16 v0, v0
	ds_read_b128 v[114:117], v77 offset:49152
	ds_read_b128 v[118:121], v77 offset:49664
	ds_read_b128 v[122:125], v77 offset:50176
	ds_read_b128 v[126:129], v77 offset:50688
	ds_read_b64 v[90:91], v74
	ds_read_b64 v[92:93], v74 offset:8
	ds_read_b64 v[94:95], v74 offset:16
	ds_read_b64 v[96:97], v73
	ds_read_b64 v[98:99], v73 offset:8
	ds_read_b64 v[100:101], v73 offset:16
	v_add_u32_e32 v1, 0x1ee00, v72
	ds_read_u16 v1, v1
	s_waitcnt vmcnt(0)
	s_waitcnt lgkmcnt(0)
	s_barrier
	s_setprio 1
	s_waitcnt lgkmcnt(0)
	v_mfma_scale_f32_32x32x64_f8f6f4 v[50:65], v[78:83], v[66:69], v[50:65], v0, v134 op_sel_hi:[0,0,0] cbsz:2 blgp:4
	v_mfma_scale_f32_32x32x64_f8f6f4 v[34:49], v[78:83], v[102:105], v[34:49], v0, v134 op_sel_hi:[0,0,0] cbsz:2 blgp:4
	v_mfma_scale_f32_32x32x64_f8f6f4 v[18:33], v[78:83], v[106:109], v[18:33], v0, v134 op_sel_hi:[0,0,0] cbsz:2 blgp:4
	v_mfma_scale_f32_32x32x64_f8f6f4 v[2:17], v[78:83], v[110:113], v[2:17], v0, v134 op_sel_hi:[0,0,0] cbsz:2 blgp:4
	v_mfma_scale_f32_32x32x64_f8f6f4 v[50:65], v[84:89], v[66:69], v[50:65], v0, v134 op_sel:[1,0,0] op_sel_hi:[0,0,0] cbsz:2 blgp:4
	v_mfma_scale_f32_32x32x64_f8f6f4 v[34:49], v[84:89], v[102:105], v[34:49], v0, v134 op_sel:[1,0,0] op_sel_hi:[0,0,0] cbsz:2 blgp:4
	v_mfma_scale_f32_32x32x64_f8f6f4 v[18:33], v[84:89], v[106:109], v[18:33], v0, v134 op_sel:[1,0,0] op_sel_hi:[0,0,0] cbsz:2 blgp:4
	v_mfma_scale_f32_32x32x64_f8f6f4 v[2:17], v[84:89], v[110:113], v[2:17], v0, v134 op_sel:[1,0,0] op_sel_hi:[0,0,0] cbsz:2 blgp:4
	v_lshrrev_b32_e32 v0, 8, v1
	v_mfma_scale_f32_32x32x64_f8f6f4 v[50:65], v[90:95], v[114:117], v[50:65], v1, v134 op_sel_hi:[0,0,0] cbsz:2 blgp:4
	v_mfma_scale_f32_32x32x64_f8f6f4 v[34:49], v[90:95], v[118:121], v[34:49], v1, v134 op_sel_hi:[0,0,0] cbsz:2 blgp:4
	v_mfma_scale_f32_32x32x64_f8f6f4 v[18:33], v[90:95], v[122:125], v[18:33], v1, v134 op_sel_hi:[0,0,0] cbsz:2 blgp:4
	v_mfma_scale_f32_32x32x64_f8f6f4 v[2:17], v[90:95], v[126:129], v[2:17], v1, v134 op_sel_hi:[0,0,0] cbsz:2 blgp:4
	v_mfma_scale_f32_32x32x64_f8f6f4 v[50:65], v[96:101], v[114:117], v[50:65], v0, v134 op_sel_hi:[0,0,0] cbsz:2 blgp:4
	v_mfma_scale_f32_32x32x64_f8f6f4 v[34:49], v[96:101], v[118:121], v[34:49], v0, v134 op_sel_hi:[0,0,0] cbsz:2 blgp:4
	v_mfma_scale_f32_32x32x64_f8f6f4 v[18:33], v[96:101], v[122:125], v[18:33], v0, v134 op_sel_hi:[0,0,0] cbsz:2 blgp:4
	v_mfma_scale_f32_32x32x64_f8f6f4 v[2:17], v[96:101], v[126:129], v[2:17], v0, v134 op_sel_hi:[0,0,0] cbsz:2 blgp:4
	s_setprio 0
	s_barrier
	s_cmpk_gt_u32 s33, 0xff
	s_cbranch_scc1 .LBB1_6
	s_barrier
